# out-GEMM epilogue: residual loads issued four row groups ahead (counted vmcnt) on top of the PEER u-side rewrite
# baseline (speedup 1.0000x reference)
.LBB0_1292:
	v_lshl_add_u32 v148, s62, 8, v1
	v_lshl_or_b32 v146, s16, 8, v151
	v_ashrrev_i32_e32 v149, 31, v148
	v_ashrrev_i32_e32 v147, 31, v146
	v_lshlrev_b64 v[156:157], 12, v[148:149]
	v_lshl_add_u64 v[164:165], v[156:157], 0, v[146:147]
	v_lshl_add_u64 v[166:167], v[164:165], 2, s[10:11]
	v_mov_b32_e32 v222, v166
	v_mov_b32_e32 v223, v167
	s_mov_b32 s99, 0
	global_load_dwordx4 v[172:175], v[222:223], off
	global_load_dwordx4 v[176:179], v[222:223], off offset:16
	global_load_dwordx4 v[180:183], v[222:223], off offset:512
	global_load_dwordx4 v[184:187], v[222:223], off offset:528
	s_mov_b32 s98, 0x40000
	v_lshl_add_u64 v[220:221], v[222:223], 0, s[98:99]
	global_load_dwordx4 v[188:191], v[220:221], off
	global_load_dwordx4 v[192:195], v[220:221], off offset:16
	global_load_dwordx4 v[196:199], v[220:221], off offset:512
	global_load_dwordx4 v[200:203], v[220:221], off offset:528
	s_mov_b32 s98, 0x80000
	v_lshl_add_u64 v[220:221], v[222:223], 0, s[98:99]
	global_load_dwordx4 v[204:207], v[220:221], off
	global_load_dwordx4 v[208:211], v[220:221], off offset:16
	global_load_dwordx4 v[212:215], v[220:221], off offset:512
	global_load_dwordx4 v[216:219], v[220:221], off offset:528
	s_mov_b32 s98, 0xc0000
	v_lshl_add_u64 v[220:221], v[222:223], 0, s[98:99]
	global_load_dwordx4 v[240:243], v[220:221], off
	global_load_dwordx4 v[244:247], v[220:221], off offset:16
	global_load_dwordx4 v[248:251], v[220:221], off offset:512
	global_load_dwordx4 v[252:255], v[220:221], off offset:528
	s_waitcnt vmcnt(12)
	v_lshl_add_u64 v[164:165], v[164:165], 1, s[20:21]
	s_lshl_b32 s34, s16, 2
	s_ashr_i32 s35, s34, 31
	v_pk_add_f32 v[168:169], v[124:125], v[174:175]
	v_pk_add_f32 v[170:171], v[122:123], v[172:173]
	v_pk_add_f32 v[128:129], v[128:129], v[178:179]
	v_pk_add_f32 v[160:161], v[126:127], v[176:177]
	v_cvt_pk_bf16_f32 v122, v170, v171
	v_cvt_pk_bf16_f32 v123, v168, v169
	v_cvt_pk_bf16_f32 v124, v160, v161
	v_cvt_pk_bf16_f32 v125, v128, v129
	global_store_dwordx4 v[164:165], v[122:125], off
	s_nop 1
	s_nop 0
	v_and_b32_e32 v123, 64, v155
	v_xor_b32_e32 v122, 16, v155
	v_add_u32_e32 v123, 64, v123
	v_xor_b32_e32 v162, 32, v155
	v_cmp_lt_i32_e32 vcc, v122, v123
	v_mul_f32_e32 v163, v169, v169
	v_mul_f32_e32 v161, v161, v161
	v_cndmask_b32_e32 v122, v155, v122, vcc
	v_cmp_lt_i32_e32 vcc, v162, v123
	v_mul_f32_e32 v129, v129, v129
	v_fmac_f32_e32 v163, v168, v168
	v_cndmask_b32_e32 v123, v155, v162, vcc
	v_mul_f32_e32 v162, v171, v171
	v_fmac_f32_e32 v162, v170, v170
	v_fmac_f32_e32 v161, v160, v160
	v_fmac_f32_e32 v129, v128, v128
	v_add_f32_e32 v128, v162, v163
	v_add_f32_e32 v129, v161, v129
	v_add_f32_e32 v128, v128, v129
	v_lshlrev_b32_e32 v122, 2, v122
	v_pk_add_f32 v[120:121], v[120:121], v[182:183]
	v_pk_add_f32 v[118:119], v[118:119], v[180:181]
	v_pk_add_f32 v[124:125], v[116:117], v[186:187]
	v_pk_add_f32 v[126:127], v[114:115], v[184:185]
	v_mul_f32_e32 v114, v119, v119
	v_mul_f32_e32 v115, v121, v121
	v_mul_f32_e32 v116, v127, v127
	v_mul_f32_e32 v117, v125, v125
	v_fmac_f32_e32 v114, v118, v118
	v_fmac_f32_e32 v115, v120, v120
	v_fmac_f32_e32 v116, v126, v126
	v_fmac_f32_e32 v117, v124, v124
	v_add_f32_e32 v114, v114, v115
	v_add_f32_e32 v115, v116, v117
	v_add_f32_e32 v114, v114, v115
	v_add_f32_e32 v114, v128, v114
	ds_bpermute_b32 v115, v122, v114
	v_lshlrev_b32_e32 v116, 2, v123
	v_cvt_pk_bf16_f32 v118, v118, v119
	v_cvt_pk_bf16_f32 v119, v120, v121
	v_cvt_pk_bf16_f32 v120, v126, v127
	s_waitcnt lgkmcnt(0)
	v_add_f32_e32 v114, v114, v115
	ds_bpermute_b32 v115, v116, v114
	v_cvt_pk_bf16_f32 v121, v124, v125
	global_store_dwordx4 v[164:165], v[118:121], off offset:256
	s_nop 1
	s_and_saveexec_b64 s[36:37], s[2:3]
	s_cbranch_execz .LBB0_1294
	v_lshlrev_b64 v[118:119], 8, v[148:149]
	v_lshl_add_u64 v[118:119], s[22:23], 0, v[118:119]
	v_lshl_add_u64 v[118:119], s[34:35], 2, v[118:119]
	s_lshl_b32 s16, s50, 2
	v_lshl_add_u64 v[118:119], v[118:119], 0, s[16:17]
	s_waitcnt lgkmcnt(0)
	v_add_f32_e32 v114, v114, v115
	global_store_dword v[118:119], v114, off
.LBB0_1294:
	s_or_b64 exec, exec, s[36:37]
	v_or_b32_e32 v114, 16, v148
	s_waitcnt lgkmcnt(0)
	v_ashrrev_i32_e32 v115, 31, v114
	v_lshlrev_b64 v[118:119], 12, v[114:115]
	v_lshl_add_u64 v[128:129], v[118:119], 0, v[146:147]
	v_lshl_add_u64 v[156:157], v[128:129], 2, s[10:11]
	s_mov_b32 s98, 0x200000
	v_lshl_add_u64 v[220:221], v[222:223], 0, s[98:99]
	global_load_dwordx4 v[172:175], v[220:221], off
	global_load_dwordx4 v[176:179], v[220:221], off offset:16
	global_load_dwordx4 v[180:183], v[220:221], off offset:512
	global_load_dwordx4 v[184:187], v[220:221], off offset:528
	s_waitcnt vmcnt(15)
	v_lshl_add_u64 v[128:129], v[128:129], 1, s[20:21]
	v_pk_add_f32 v[120:121], v[112:113], v[190:191]
	v_pk_add_f32 v[118:119], v[110:111], v[188:189]
	v_pk_add_f32 v[126:127], v[108:109], v[194:195]
	v_pk_add_f32 v[124:125], v[106:107], v[192:193]
	v_cvt_pk_bf16_f32 v106, v118, v119
	v_cvt_pk_bf16_f32 v107, v120, v121
	v_cvt_pk_bf16_f32 v108, v124, v125
	v_cvt_pk_bf16_f32 v109, v126, v127
	global_store_dwordx4 v[128:129], v[106:109], off
	s_nop 1
	s_nop 0
	v_mul_f32_e32 v117, v119, v119
	v_mul_f32_e32 v119, v121, v121
	v_mul_f32_e32 v121, v125, v125
	v_mul_f32_e32 v123, v127, v127
	v_fmac_f32_e32 v117, v118, v118
	v_fmac_f32_e32 v119, v120, v120
	v_fmac_f32_e32 v121, v124, v124
	v_fmac_f32_e32 v123, v126, v126
	v_add_f32_e32 v117, v117, v119
	v_add_f32_e32 v118, v121, v123
	v_add_f32_e32 v117, v117, v118
	v_pk_add_f32 v[104:105], v[104:105], v[198:199]
	v_pk_add_f32 v[102:103], v[102:103], v[196:197]
	v_pk_add_f32 v[106:107], v[100:101], v[202:203]
	v_pk_add_f32 v[108:109], v[98:99], v[200:201]
	v_mul_f32_e32 v98, v103, v103
	v_mul_f32_e32 v99, v105, v105
	v_mul_f32_e32 v100, v109, v109
	v_mul_f32_e32 v101, v107, v107
	v_fmac_f32_e32 v98, v102, v102
	v_fmac_f32_e32 v99, v104, v104
	v_fmac_f32_e32 v100, v108, v108
	v_fmac_f32_e32 v101, v106, v106
	v_add_f32_e32 v98, v98, v99
	v_add_f32_e32 v99, v100, v101
	v_add_f32_e32 v98, v98, v99
	v_add_f32_e32 v98, v117, v98
	ds_bpermute_b32 v99, v122, v98
	v_cvt_pk_bf16_f32 v100, v102, v103
	v_cvt_pk_bf16_f32 v101, v104, v105
	v_cvt_pk_bf16_f32 v102, v108, v109
	v_cvt_pk_bf16_f32 v103, v106, v107
	s_waitcnt lgkmcnt(0)
	v_add_f32_e32 v98, v98, v99
	ds_bpermute_b32 v99, v116, v98
	global_store_dwordx4 v[128:129], v[100:103], off offset:256
	s_nop 1
	s_and_saveexec_b64 s[36:37], s[2:3]
	s_cbranch_execz .LBB0_1296
	v_lshlrev_b64 v[100:101], 8, v[114:115]
	v_lshl_add_u64 v[100:101], s[22:23], 0, v[100:101]
	v_lshl_add_u64 v[100:101], s[34:35], 2, v[100:101]
	s_lshl_b32 s16, s50, 2
	v_lshl_add_u64 v[100:101], v[100:101], 0, s[16:17]
	s_waitcnt lgkmcnt(0)
	v_add_f32_e32 v98, v98, v99
	global_store_dword v[100:101], v98, off
.LBB0_1296:
	s_or_b64 exec, exec, s[36:37]
	v_or_b32_e32 v98, 32, v148
	s_waitcnt lgkmcnt(0)
	v_ashrrev_i32_e32 v99, 31, v98
	v_lshlrev_b64 v[100:101], 12, v[98:99]
	v_lshl_add_u64 v[108:109], v[100:101], 0, v[146:147]
	v_lshl_add_u64 v[110:111], v[108:109], 2, s[10:11]
	s_mov_b32 s98, 0x240000
	v_lshl_add_u64 v[220:221], v[222:223], 0, s[98:99]
	global_load_dwordx4 v[188:191], v[220:221], off
	global_load_dwordx4 v[192:195], v[220:221], off offset:16
	global_load_dwordx4 v[196:199], v[220:221], off offset:512
	global_load_dwordx4 v[200:203], v[220:221], off offset:528
	s_waitcnt vmcnt(18)
	v_lshl_add_u64 v[108:109], v[108:109], 1, s[20:21]
	v_pk_add_f32 v[102:103], v[96:97], v[206:207]
	v_pk_add_f32 v[100:101], v[94:95], v[204:205]
	v_pk_add_f32 v[106:107], v[92:93], v[210:211]
	v_pk_add_f32 v[104:105], v[90:91], v[208:209]
	v_cvt_pk_bf16_f32 v90, v100, v101
	v_cvt_pk_bf16_f32 v91, v102, v103
	v_cvt_pk_bf16_f32 v92, v104, v105
	v_cvt_pk_bf16_f32 v93, v106, v107
	global_store_dwordx4 v[108:109], v[90:93], off
	s_nop 1
	s_nop 0
	v_mul_f32_e32 v101, v101, v101
	v_mul_f32_e32 v103, v103, v103
	v_mul_f32_e32 v105, v105, v105
	v_mul_f32_e32 v107, v107, v107
	v_fmac_f32_e32 v101, v100, v100
	v_fmac_f32_e32 v103, v102, v102
	v_fmac_f32_e32 v105, v104, v104
	v_fmac_f32_e32 v107, v106, v106
	v_add_f32_e32 v100, v101, v103
	v_add_f32_e32 v101, v105, v107
	v_add_f32_e32 v100, v100, v101
	v_pk_add_f32 v[88:89], v[88:89], v[214:215]
	v_pk_add_f32 v[86:87], v[86:87], v[212:213]
	v_pk_add_f32 v[90:91], v[84:85], v[218:219]
	v_pk_add_f32 v[92:93], v[82:83], v[216:217]
	v_mul_f32_e32 v82, v87, v87
	v_mul_f32_e32 v83, v89, v89
	v_mul_f32_e32 v84, v93, v93
	v_mul_f32_e32 v85, v91, v91
	v_fmac_f32_e32 v82, v86, v86
	v_fmac_f32_e32 v83, v88, v88
	v_fmac_f32_e32 v84, v92, v92
	v_fmac_f32_e32 v85, v90, v90
	v_add_f32_e32 v82, v82, v83
	v_add_f32_e32 v83, v84, v85
	v_add_f32_e32 v82, v82, v83
	v_add_f32_e32 v82, v100, v82
	ds_bpermute_b32 v83, v122, v82
	v_cvt_pk_bf16_f32 v84, v86, v87
	v_cvt_pk_bf16_f32 v85, v88, v89
	v_cvt_pk_bf16_f32 v86, v92, v93
	v_cvt_pk_bf16_f32 v87, v90, v91
	s_waitcnt lgkmcnt(0)
	v_add_f32_e32 v82, v82, v83
	ds_bpermute_b32 v83, v116, v82
	global_store_dwordx4 v[108:109], v[84:87], off offset:256
	s_nop 1
	s_and_saveexec_b64 s[36:37], s[2:3]
	s_cbranch_execz .LBB0_1298
	v_lshlrev_b64 v[84:85], 8, v[98:99]
	v_lshl_add_u64 v[84:85], s[22:23], 0, v[84:85]
	v_lshl_add_u64 v[84:85], s[34:35], 2, v[84:85]
	s_lshl_b32 s16, s50, 2
	v_lshl_add_u64 v[84:85], v[84:85], 0, s[16:17]
	s_waitcnt lgkmcnt(0)
	v_add_f32_e32 v82, v82, v83
	global_store_dword v[84:85], v82, off
.LBB0_1298:
	s_or_b64 exec, exec, s[36:37]
	v_or_b32_e32 v82, 48, v148
	s_waitcnt lgkmcnt(0)
	v_ashrrev_i32_e32 v83, 31, v82
	v_lshlrev_b64 v[84:85], 12, v[82:83]
	v_lshl_add_u64 v[92:93], v[84:85], 0, v[146:147]
	v_lshl_add_u64 v[94:95], v[92:93], 2, s[10:11]
	s_mov_b32 s98, 0x280000
	v_lshl_add_u64 v[220:221], v[222:223], 0, s[98:99]
	global_load_dwordx4 v[204:207], v[220:221], off
	global_load_dwordx4 v[208:211], v[220:221], off offset:16
	global_load_dwordx4 v[212:215], v[220:221], off offset:512
	global_load_dwordx4 v[216:219], v[220:221], off offset:528
	s_waitcnt vmcnt(21)
	v_lshl_add_u64 v[92:93], v[92:93], 1, s[20:21]
	v_pk_add_f32 v[86:87], v[80:81], v[242:243]
	v_pk_add_f32 v[84:85], v[78:79], v[240:241]
	v_pk_add_f32 v[90:91], v[76:77], v[246:247]
	v_pk_add_f32 v[88:89], v[74:75], v[244:245]
	v_cvt_pk_bf16_f32 v74, v84, v85
	v_cvt_pk_bf16_f32 v75, v86, v87
	v_cvt_pk_bf16_f32 v76, v88, v89
	v_cvt_pk_bf16_f32 v77, v90, v91
	global_store_dwordx4 v[92:93], v[74:77], off
	s_nop 1
	s_nop 0
	v_mul_f32_e32 v85, v85, v85
	v_mul_f32_e32 v87, v87, v87
	v_mul_f32_e32 v89, v89, v89
	v_mul_f32_e32 v91, v91, v91
	v_fmac_f32_e32 v85, v84, v84
	v_fmac_f32_e32 v87, v86, v86
	v_fmac_f32_e32 v89, v88, v88
	v_fmac_f32_e32 v91, v90, v90
	v_add_f32_e32 v84, v85, v87
	v_add_f32_e32 v85, v89, v91
	v_add_f32_e32 v84, v84, v85
	v_pk_add_f32 v[72:73], v[72:73], v[250:251]
	v_pk_add_f32 v[70:71], v[70:71], v[248:249]
	v_pk_add_f32 v[74:75], v[68:69], v[254:255]
	v_pk_add_f32 v[76:77], v[66:67], v[252:253]
	v_mul_f32_e32 v66, v71, v71
	v_mul_f32_e32 v67, v73, v73
	v_mul_f32_e32 v68, v77, v77
	v_mul_f32_e32 v69, v75, v75
	v_fmac_f32_e32 v66, v70, v70
	v_fmac_f32_e32 v67, v72, v72
	v_fmac_f32_e32 v68, v76, v76
	v_fmac_f32_e32 v69, v74, v74
	v_add_f32_e32 v66, v66, v67
	v_add_f32_e32 v67, v68, v69
	v_add_f32_e32 v66, v66, v67
	v_add_f32_e32 v66, v84, v66
	ds_bpermute_b32 v67, v122, v66
	v_cvt_pk_bf16_f32 v68, v70, v71
	v_cvt_pk_bf16_f32 v69, v72, v73
	v_cvt_pk_bf16_f32 v70, v76, v77
	v_cvt_pk_bf16_f32 v71, v74, v75
	s_waitcnt lgkmcnt(0)
	v_add_f32_e32 v66, v66, v67
	ds_bpermute_b32 v67, v116, v66
	global_store_dwordx4 v[92:93], v[68:71], off offset:256
	s_nop 1
	s_and_saveexec_b64 s[36:37], s[2:3]
	s_cbranch_execz .LBB0_1300
	v_lshlrev_b64 v[68:69], 8, v[82:83]
	v_lshl_add_u64 v[68:69], s[22:23], 0, v[68:69]
	v_lshl_add_u64 v[68:69], s[34:35], 2, v[68:69]
	s_lshl_b32 s16, s50, 2
	v_lshl_add_u64 v[68:69], v[68:69], 0, s[16:17]
	s_waitcnt lgkmcnt(0)
	v_add_f32_e32 v66, v66, v67
	global_store_dword v[68:69], v66, off
.LBB0_1300:
	s_or_b64 exec, exec, s[36:37]
	v_add_u32_e32 v66, 0x80, v148
	s_waitcnt lgkmcnt(0)
	v_ashrrev_i32_e32 v67, 31, v66
	v_lshlrev_b64 v[68:69], 12, v[66:67]
	v_lshl_add_u64 v[76:77], v[68:69], 0, v[146:147]
	v_lshl_add_u64 v[78:79], v[76:77], 2, s[10:11]
	s_mov_b32 s98, 0x2c0000
	v_lshl_add_u64 v[220:221], v[222:223], 0, s[98:99]
	global_load_dwordx4 v[240:243], v[220:221], off
	global_load_dwordx4 v[244:247], v[220:221], off offset:16
	global_load_dwordx4 v[248:251], v[220:221], off offset:512
	global_load_dwordx4 v[252:255], v[220:221], off offset:528
	s_waitcnt vmcnt(21)
	v_lshl_add_u64 v[76:77], v[76:77], 1, s[20:21]
	v_pk_add_f32 v[70:71], v[64:65], v[174:175]
	v_pk_add_f32 v[68:69], v[62:63], v[172:173]
	v_pk_add_f32 v[74:75], v[60:61], v[178:179]
	v_pk_add_f32 v[72:73], v[58:59], v[176:177]
	v_cvt_pk_bf16_f32 v58, v68, v69
	v_cvt_pk_bf16_f32 v59, v70, v71
	v_cvt_pk_bf16_f32 v60, v72, v73
	v_cvt_pk_bf16_f32 v61, v74, v75
	global_store_dwordx4 v[76:77], v[58:61], off
	s_nop 1
	s_nop 0
	v_mul_f32_e32 v69, v69, v69
	v_mul_f32_e32 v71, v71, v71
	v_mul_f32_e32 v73, v73, v73
	v_mul_f32_e32 v75, v75, v75
	v_fmac_f32_e32 v69, v68, v68
	v_fmac_f32_e32 v71, v70, v70
	v_fmac_f32_e32 v73, v72, v72
	v_fmac_f32_e32 v75, v74, v74
	v_add_f32_e32 v68, v69, v71
	v_add_f32_e32 v69, v73, v75
	v_add_f32_e32 v68, v68, v69
	v_pk_add_f32 v[56:57], v[56:57], v[182:183]
	v_pk_add_f32 v[54:55], v[54:55], v[180:181]
	v_pk_add_f32 v[58:59], v[52:53], v[186:187]
	v_pk_add_f32 v[60:61], v[50:51], v[184:185]
	v_mul_f32_e32 v50, v55, v55
	v_mul_f32_e32 v51, v57, v57
	v_mul_f32_e32 v52, v61, v61
	v_mul_f32_e32 v53, v59, v59
	v_fmac_f32_e32 v50, v54, v54
	v_fmac_f32_e32 v51, v56, v56
	v_fmac_f32_e32 v52, v60, v60
	v_fmac_f32_e32 v53, v58, v58
	v_add_f32_e32 v50, v50, v51
	v_add_f32_e32 v51, v52, v53
	v_add_f32_e32 v50, v50, v51
	v_add_f32_e32 v50, v68, v50
	ds_bpermute_b32 v51, v122, v50
	v_cvt_pk_bf16_f32 v52, v54, v55
	v_cvt_pk_bf16_f32 v53, v56, v57
	v_cvt_pk_bf16_f32 v54, v60, v61
	v_cvt_pk_bf16_f32 v55, v58, v59
	s_waitcnt lgkmcnt(0)
	v_add_f32_e32 v50, v50, v51
	ds_bpermute_b32 v51, v116, v50
	global_store_dwordx4 v[76:77], v[52:55], off offset:256
	s_nop 1
	s_and_saveexec_b64 s[36:37], s[2:3]
	s_cbranch_execz .LBB0_1302
	v_lshlrev_b64 v[52:53], 8, v[66:67]
	v_lshl_add_u64 v[52:53], s[22:23], 0, v[52:53]
	v_lshl_add_u64 v[52:53], s[34:35], 2, v[52:53]
	s_lshl_b32 s16, s50, 2
	v_lshl_add_u64 v[52:53], v[52:53], 0, s[16:17]
	s_waitcnt lgkmcnt(0)
	v_add_f32_e32 v50, v50, v51
	global_store_dword v[52:53], v50, off
.LBB0_1302:
	s_or_b64 exec, exec, s[36:37]
	v_add_u32_e32 v50, 0x90, v148
	s_waitcnt lgkmcnt(0)
	v_ashrrev_i32_e32 v51, 31, v50
	v_lshlrev_b64 v[52:53], 12, v[50:51]
	v_lshl_add_u64 v[60:61], v[52:53], 0, v[146:147]
	v_lshl_add_u64 v[62:63], v[60:61], 2, s[10:11]
	s_waitcnt vmcnt(17)
	v_lshl_add_u64 v[60:61], v[60:61], 1, s[20:21]
	v_pk_add_f32 v[54:55], v[48:49], v[190:191]
	v_pk_add_f32 v[52:53], v[46:47], v[188:189]
	v_pk_add_f32 v[58:59], v[44:45], v[194:195]
	v_pk_add_f32 v[56:57], v[42:43], v[192:193]
	v_cvt_pk_bf16_f32 v42, v52, v53
	v_cvt_pk_bf16_f32 v43, v54, v55
	v_cvt_pk_bf16_f32 v44, v56, v57
	v_cvt_pk_bf16_f32 v45, v58, v59
	global_store_dwordx4 v[60:61], v[42:45], off
	s_nop 1
	s_nop 0
	v_mul_f32_e32 v53, v53, v53
	v_mul_f32_e32 v55, v55, v55
	v_mul_f32_e32 v57, v57, v57
	v_mul_f32_e32 v59, v59, v59
	v_fmac_f32_e32 v53, v52, v52
	v_fmac_f32_e32 v55, v54, v54
	v_fmac_f32_e32 v57, v56, v56
	v_fmac_f32_e32 v59, v58, v58
	v_add_f32_e32 v52, v53, v55
	v_add_f32_e32 v53, v57, v59
	v_add_f32_e32 v52, v52, v53
	v_pk_add_f32 v[40:41], v[40:41], v[198:199]
	v_pk_add_f32 v[38:39], v[38:39], v[196:197]
	v_pk_add_f32 v[42:43], v[36:37], v[202:203]
	v_pk_add_f32 v[44:45], v[34:35], v[200:201]
	v_mul_f32_e32 v34, v39, v39
	v_mul_f32_e32 v35, v41, v41
	v_mul_f32_e32 v36, v45, v45
	v_mul_f32_e32 v37, v43, v43
	v_fmac_f32_e32 v34, v38, v38
	v_fmac_f32_e32 v35, v40, v40
	v_fmac_f32_e32 v36, v44, v44
	v_fmac_f32_e32 v37, v42, v42
	v_add_f32_e32 v34, v34, v35
	v_add_f32_e32 v35, v36, v37
	v_add_f32_e32 v34, v34, v35
	v_add_f32_e32 v34, v52, v34
	ds_bpermute_b32 v35, v122, v34
	v_cvt_pk_bf16_f32 v36, v38, v39
	v_cvt_pk_bf16_f32 v37, v40, v41
	v_cvt_pk_bf16_f32 v38, v44, v45
	v_cvt_pk_bf16_f32 v39, v42, v43
	s_waitcnt lgkmcnt(0)
	v_add_f32_e32 v34, v34, v35
	ds_bpermute_b32 v35, v116, v34
	global_store_dwordx4 v[60:61], v[36:39], off offset:256
	s_nop 1
	s_and_saveexec_b64 s[36:37], s[2:3]
	s_cbranch_execz .LBB0_1304
	v_lshlrev_b64 v[36:37], 8, v[50:51]
	v_lshl_add_u64 v[36:37], s[22:23], 0, v[36:37]
	v_lshl_add_u64 v[36:37], s[34:35], 2, v[36:37]
	s_lshl_b32 s16, s50, 2
	v_lshl_add_u64 v[36:37], v[36:37], 0, s[16:17]
	s_waitcnt lgkmcnt(0)
	v_add_f32_e32 v34, v34, v35
	global_store_dword v[36:37], v34, off
.LBB0_1304:
	s_or_b64 exec, exec, s[36:37]
	v_add_u32_e32 v34, 0xa0, v148
	s_waitcnt lgkmcnt(0)
	v_ashrrev_i32_e32 v35, 31, v34
	v_lshlrev_b64 v[36:37], 12, v[34:35]
	v_lshl_add_u64 v[44:45], v[36:37], 0, v[146:147]
	v_lshl_add_u64 v[46:47], v[44:45], 2, s[10:11]
	s_waitcnt vmcnt(13)
	v_lshl_add_u64 v[44:45], v[44:45], 1, s[20:21]
	v_pk_add_f32 v[38:39], v[32:33], v[206:207]
	v_pk_add_f32 v[36:37], v[30:31], v[204:205]
	v_pk_add_f32 v[42:43], v[28:29], v[210:211]
	v_pk_add_f32 v[40:41], v[26:27], v[208:209]
	v_cvt_pk_bf16_f32 v26, v36, v37
	v_cvt_pk_bf16_f32 v27, v38, v39
	v_cvt_pk_bf16_f32 v28, v40, v41
	v_cvt_pk_bf16_f32 v29, v42, v43
	global_store_dwordx4 v[44:45], v[26:29], off
	s_nop 1
	s_nop 0
	v_mul_f32_e32 v37, v37, v37
	v_mul_f32_e32 v39, v39, v39
	v_mul_f32_e32 v41, v41, v41
	v_mul_f32_e32 v43, v43, v43
	v_fmac_f32_e32 v37, v36, v36
	v_fmac_f32_e32 v39, v38, v38
	v_fmac_f32_e32 v41, v40, v40
	v_fmac_f32_e32 v43, v42, v42
	v_add_f32_e32 v36, v37, v39
	v_add_f32_e32 v37, v41, v43
	v_add_f32_e32 v36, v36, v37
	v_pk_add_f32 v[24:25], v[24:25], v[214:215]
	v_pk_add_f32 v[22:23], v[22:23], v[212:213]
	v_pk_add_f32 v[26:27], v[20:21], v[218:219]
	v_pk_add_f32 v[28:29], v[18:19], v[216:217]
	v_mul_f32_e32 v18, v23, v23
	v_mul_f32_e32 v19, v25, v25
	v_mul_f32_e32 v20, v29, v29
	v_mul_f32_e32 v21, v27, v27
	v_fmac_f32_e32 v18, v22, v22
	v_fmac_f32_e32 v19, v24, v24
	v_fmac_f32_e32 v20, v28, v28
	v_fmac_f32_e32 v21, v26, v26
	v_add_f32_e32 v18, v18, v19
	v_add_f32_e32 v19, v20, v21
	v_add_f32_e32 v18, v18, v19
	v_add_f32_e32 v18, v36, v18
	ds_bpermute_b32 v19, v122, v18
	v_cvt_pk_bf16_f32 v20, v22, v23
	v_cvt_pk_bf16_f32 v21, v24, v25
	v_cvt_pk_bf16_f32 v22, v28, v29
	v_cvt_pk_bf16_f32 v23, v26, v27
	s_waitcnt lgkmcnt(0)
	v_add_f32_e32 v18, v18, v19
	ds_bpermute_b32 v19, v116, v18
	global_store_dwordx4 v[44:45], v[20:23], off offset:256
	s_nop 1
	s_and_saveexec_b64 s[36:37], s[2:3]
	s_cbranch_execz .LBB0_1306
	v_lshlrev_b64 v[20:21], 8, v[34:35]
	v_lshl_add_u64 v[20:21], s[22:23], 0, v[20:21]
	v_lshl_add_u64 v[20:21], s[34:35], 2, v[20:21]
	s_lshl_b32 s16, s50, 2
	v_lshl_add_u64 v[20:21], v[20:21], 0, s[16:17]
	s_waitcnt lgkmcnt(0)
	v_add_f32_e32 v18, v18, v19
	global_store_dword v[20:21], v18, off
.LBB0_1306:
	s_or_b64 exec, exec, s[36:37]
	v_add_u32_e32 v18, 0xb0, v148
	s_waitcnt lgkmcnt(0)
	v_ashrrev_i32_e32 v19, 31, v18
	v_lshlrev_b64 v[20:21], 12, v[18:19]
	v_lshl_add_u64 v[28:29], v[20:21], 0, v[146:147]
	v_lshl_add_u64 v[30:31], v[28:29], 2, s[10:11]
	s_waitcnt vmcnt(9)
	v_lshl_add_u64 v[28:29], v[28:29], 1, s[20:21]
	v_pk_add_f32 v[22:23], v[16:17], v[242:243]
	v_pk_add_f32 v[20:21], v[14:15], v[240:241]
	v_pk_add_f32 v[26:27], v[12:13], v[246:247]
	v_pk_add_f32 v[24:25], v[10:11], v[244:245]
	v_cvt_pk_bf16_f32 v10, v20, v21
	v_cvt_pk_bf16_f32 v11, v22, v23
	v_cvt_pk_bf16_f32 v12, v24, v25
	v_cvt_pk_bf16_f32 v13, v26, v27
	global_store_dwordx4 v[28:29], v[10:13], off
	s_nop 1
	s_nop 0
	v_mul_f32_e32 v21, v21, v21
	v_mul_f32_e32 v23, v23, v23
	v_mul_f32_e32 v25, v25, v25
	v_mul_f32_e32 v27, v27, v27
	v_fmac_f32_e32 v21, v20, v20
	v_fmac_f32_e32 v23, v22, v22
	v_fmac_f32_e32 v25, v24, v24
	v_fmac_f32_e32 v27, v26, v26
	v_add_f32_e32 v20, v21, v23
	v_add_f32_e32 v21, v25, v27
	v_add_f32_e32 v20, v20, v21
	v_pk_add_f32 v[8:9], v[8:9], v[250:251]
	v_pk_add_f32 v[6:7], v[6:7], v[248:249]
	v_pk_add_f32 v[10:11], v[4:5], v[254:255]
	v_pk_add_f32 v[12:13], v[2:3], v[252:253]
	v_mul_f32_e32 v2, v7, v7
	v_mul_f32_e32 v3, v9, v9
	v_mul_f32_e32 v4, v13, v13
	v_mul_f32_e32 v5, v11, v11
	v_fmac_f32_e32 v2, v6, v6
	v_fmac_f32_e32 v3, v8, v8
	v_fmac_f32_e32 v4, v12, v12
	v_fmac_f32_e32 v5, v10, v10
	v_add_f32_e32 v2, v2, v3
	v_add_f32_e32 v3, v4, v5
	v_add_f32_e32 v2, v2, v3
	v_add_f32_e32 v2, v20, v2
	ds_bpermute_b32 v3, v122, v2
	v_cvt_pk_bf16_f32 v4, v6, v7
	v_cvt_pk_bf16_f32 v5, v8, v9
	v_cvt_pk_bf16_f32 v6, v12, v13
	v_cvt_pk_bf16_f32 v7, v10, v11
	s_waitcnt lgkmcnt(0)
	v_add_f32_e32 v2, v2, v3
	ds_bpermute_b32 v3, v116, v2
	global_store_dwordx4 v[28:29], v[4:7], off offset:256
	s_nop 1
	s_and_saveexec_b64 s[36:37], s[2:3]
	s_cbranch_execz .LBB0_1308
	v_lshlrev_b64 v[4:5], 8, v[18:19]
	v_lshl_add_u64 v[4:5], s[22:23], 0, v[4:5]
	v_lshl_add_u64 v[4:5], s[34:35], 2, v[4:5]
	s_lshl_b32 s16, s50, 2
	v_lshl_add_u64 v[4:5], v[4:5], 0, s[16:17]
	s_waitcnt lgkmcnt(0)
	v_add_f32_e32 v2, v2, v3
	global_store_dword v[4:5], v2, off

	.amdhsa_kernel _Z6mk_fwd4Args
		.amdhsa_group_segment_fixed_size 0
		.amdhsa_private_segment_fixed_size 0
		.amdhsa_kernarg_size 472
		.amdhsa_user_sgpr_count 2
		.amdhsa_user_sgpr_dispatch_ptr 0
		.amdhsa_user_sgpr_queue_ptr 0
		.amdhsa_user_sgpr_kernarg_segment_ptr 1
		.amdhsa_user_sgpr_dispatch_id 0
		.amdhsa_user_sgpr_kernarg_preload_length 0
		.amdhsa_user_sgpr_kernarg_preload_offset 0
		.amdhsa_user_sgpr_private_segment_size 0
		.amdhsa_uses_dynamic_stack 0
		.amdhsa_enable_private_segment 0
		.amdhsa_system_sgpr_workgroup_id_x 1
		.amdhsa_system_sgpr_workgroup_id_y 0
		.amdhsa_system_sgpr_workgroup_id_z 0
		.amdhsa_system_sgpr_workgroup_info 0
		.amdhsa_system_vgpr_workitem_id 0
		.amdhsa_next_free_vgpr 256
		.amdhsa_next_free_sgpr 102
		.amdhsa_accum_offset 256
		.amdhsa_reserve_vcc 1
		.amdhsa_float_round_mode_32 0
		.amdhsa_float_round_mode_16_64 0
		.amdhsa_float_denorm_mode_32 3
		.amdhsa_float_denorm_mode_16_64 3
		.amdhsa_dx10_clamp 1
		.amdhsa_ieee_mode 1
		.amdhsa_fp16_overflow 0
		.amdhsa_tg_split 0
		.amdhsa_exception_fp_ieee_invalid_op 0
		.amdhsa_exception_fp_denorm_src 0
		.amdhsa_exception_fp_ieee_div_zero 0
		.amdhsa_exception_fp_ieee_overflow 0
		.amdhsa_exception_fp_ieee_underflow 0
		.amdhsa_exception_fp_ieee_inexact 0
		.amdhsa_exception_int_div_zero 0
	.end_amdhsa_kernel

amdhsa.kernels:
  - .agpr_count:     0
    .args:
      - .offset:         0
        .size:           216
        .value_kind:     by_value
      - .offset:         216
        .size:           4
        .value_kind:     hidden_block_count_x
      - .offset:         220
        .size:           4
        .value_kind:     hidden_block_count_y
      - .offset:         224
        .size:           4
        .value_kind:     hidden_block_count_z
      - .offset:         228
        .size:           2
        .value_kind:     hidden_group_size_x
      - .offset:         230
        .size:           2
        .value_kind:     hidden_group_size_y
      - .offset:         232
        .size:           2
        .value_kind:     hidden_group_size_z
      - .offset:         234
        .size:           2
        .value_kind:     hidden_remainder_x
      - .offset:         236
        .size:           2
        .value_kind:     hidden_remainder_y
      - .offset:         238
        .size:           2
        .value_kind:     hidden_remainder_z
      - .offset:         256
        .size:           8
        .value_kind:     hidden_global_offset_x
      - .offset:         264
        .size:           8
        .value_kind:     hidden_global_offset_y
      - .offset:         272
        .size:           8
        .value_kind:     hidden_global_offset_z
      - .offset:         280
        .size:           2
        .value_kind:     hidden_grid_dims
      - .offset:         336
        .size:           4
        .value_kind:     hidden_dynamic_lds_size
    .group_segment_fixed_size: 0
    .kernarg_segment_align: 8
    .kernarg_segment_size: 472
    .language:       OpenCL C
    .language_version:
      - 2
      - 0
    .max_flat_workgroup_size: 512
    .name:           _Z6mk_fwd4Args
    .private_segment_fixed_size: 0
    .sgpr_count:     108
    .sgpr_spill_count: 241
    .symbol:         _Z6mk_fwd4Args.kd
    .uniform_work_group_size: 1
    .uses_dynamic_stack: false
    .vgpr_count:     256
    .vgpr_spill_count: 0
    .wavefront_size: 64
